# P7 norm2+router loop: 290 packed-f32 VALU ops (v_pk_fma/mul/add_f32) replaced by scalar pairs, same arithmetic (instruction selection 7.5), on top of v9_prohoist
# baseline (speedup 1.0000x reference)
.LBB0_1536:
	s_or_b64 exec, exec, s[0:1]
	v_and_b32_e32 v73, 0xffff0000, v62
	v_and_b32_e32 v117, 0xffff0000, v60
	v_lshlrev_b32_e32 v72, 16, v62
	v_lshlrev_b32_e32 v116, 16, v60
	v_lshlrev_b32_e32 v98, 16, v57
	v_and_b32_e32 v99, 0xffff0000, v57
	v_mul_f32_e32 v57, v73, v73
	v_mul_f32_e32 v62, v117, v117
	v_lshlrev_b32_e32 v76, 16, v63
	v_lshlrev_b32_e32 v118, 16, v61
	v_fmac_f32_e32 v57, v72, v72
	v_fmac_f32_e32 v62, v116, v116
	v_and_b32_e32 v77, 0xffff0000, v63
	v_and_b32_e32 v119, 0xffff0000, v61
	v_fmac_f32_e32 v57, v76, v76
	v_fmac_f32_e32 v62, v118, v118
	v_and_b32_e32 v109, 0xffff0000, v58
	v_fmac_f32_e32 v57, v77, v77
	v_fmac_f32_e32 v62, v119, v119
	v_lshlrev_b32_e32 v108, 16, v58
	v_add_f32_e32 v57, v57, v62
	v_mul_f32_e32 v62, v109, v109
	v_lshlrev_b32_e32 v110, 16, v59
	v_fmac_f32_e32 v62, v108, v108
	v_and_b32_e32 v111, 0xffff0000, v59
	v_fmac_f32_e32 v62, v110, v110
	v_and_b32_e32 v97, 0xffff0000, v56
	v_fmac_f32_e32 v62, v111, v111
	v_lshlrev_b32_e32 v96, 16, v56
	v_add_f32_e32 v57, v57, v62
	v_mul_f32_e32 v62, v97, v97
	v_fmac_f32_e32 v62, v96, v96
	v_fmac_f32_e32 v62, v98, v98
	v_fmac_f32_e32 v62, v99, v99
	v_add_f32_e32 v57, v57, v62
	v_add_u32_e32 v74, 8, v6
	v_cmp_gt_i32_e64 s[44:45], s20, v74
	v_add_f32_dpp v57, v57, v57 quad_perm:[1,0,3,2] row_mask:0xf bank_mask:0xf bound_ctrl:1
	s_mov_b32 s0, 0x3e0f83e1
	v_cndmask_b32_e64 v56, v6, v74, s[44:45]
	v_add_f32_dpp v57, v57, v57 quad_perm:[2,3,0,1] row_mask:0xf bank_mask:0xf bound_ctrl:1
	v_and_b32_e32 v61, 0xffff0000, v70
	v_and_b32_e32 v113, 0xffff0000, v68
	v_add_f32_dpp v57, v57, v57 row_ror:4 row_mask:0xf bank_mask:0xf bound_ctrl:1
	v_lshlrev_b32_e32 v60, 16, v70
	v_lshlrev_b32_e32 v112, 16, v68
	v_add_f32_dpp v57, v57, v57 row_ror:8 row_mask:0xf bank_mask:0xf bound_ctrl:1
	v_mov_b32_e32 v62, v57
	s_nop 1
	v_permlane16_swap_b32_e32 v57, v62
	v_add_f32_e32 v63, v57, v62
	v_mul_hi_i32 v57, v56, s0
	v_lshrrev_b32_e32 v62, 31, v57
	v_ashrrev_i32_e32 v57, 11, v57
	v_add_u32_e32 v57, v57, v62
	v_mul_i32_i24_e32 v62, 0x2100, v57
	v_lshlrev_b32_e32 v92, 16, v64
	v_and_b32_e32 v93, 0xffff0000, v64
	v_sub_u32_e32 v75, v56, v62
	v_mul_f32_e32 v62, v61, v61
	v_mul_f32_e32 v64, v113, v113
	v_lshlrev_b32_e32 v58, 16, v71
	v_lshlrev_b32_e32 v114, 16, v69
	v_fmac_f32_e32 v62, v60, v60
	v_fmac_f32_e32 v64, v112, v112
	v_and_b32_e32 v59, 0xffff0000, v71
	v_and_b32_e32 v115, 0xffff0000, v69
	v_fmac_f32_e32 v62, v58, v58
	v_fmac_f32_e32 v64, v114, v114
	v_and_b32_e32 v105, 0xffff0000, v66
	v_fmac_f32_e32 v62, v59, v59
	v_fmac_f32_e32 v64, v115, v115
	v_lshlrev_b32_e32 v104, 16, v66
	v_add_f32_e32 v62, v62, v64
	v_mul_f32_e32 v64, v105, v105
	v_lshlrev_b32_e32 v106, 16, v67
	v_fmac_f32_e32 v64, v104, v104
	v_and_b32_e32 v107, 0xffff0000, v67
	v_fmac_f32_e32 v64, v106, v106
	v_fmac_f32_e32 v64, v107, v107
	v_add_f32_e32 v62, v62, v64
	v_mul_f32_e32 v64, v93, v93
	v_lshlrev_b32_e32 v94, 16, v65
	v_fmac_f32_e32 v64, v92, v92
	v_and_b32_e32 v95, 0xffff0000, v65
	v_fmac_f32_e32 v64, v94, v94
	v_fmac_f32_e32 v64, v95, v95
	v_add_f32_e32 v62, v62, v64
	v_mov_b32_e32 v65, v63
	s_nop 1
	v_permlane32_swap_b32_e32 v63, v65
	v_add_f32_dpp v62, v62, v62 quad_perm:[1,0,3,2] row_mask:0xf bank_mask:0xf bound_ctrl:1
	v_mul_hi_i32 v2, v6, s0
	s_mov_b32 s0, 0x3a800000
	v_add_f32_dpp v62, v62, v62 quad_perm:[2,3,0,1] row_mask:0xf bank_mask:0xf bound_ctrl:1
	v_lshrrev_b32_e32 v7, 31, v2
	v_ashrrev_i32_e32 v2, 11, v2
	v_add_f32_dpp v62, v62, v62 row_ror:4 row_mask:0xf bank_mask:0xf bound_ctrl:1
	v_add_u32_e32 v2, v2, v7
	v_mul_i32_i24_e32 v7, 0x2100, v2
	v_add_f32_dpp v62, v62, v62 row_ror:8 row_mask:0xf bank_mask:0xf bound_ctrl:1
	v_mov_b32_e32 v64, v62
	s_nop 1
	v_permlane16_swap_b32_e32 v62, v64
	v_add_f32_e32 v62, v62, v64
	v_mov_b32_e32 v64, v62
	s_nop 1
	v_permlane32_swap_b32_e32 v62, v64
	v_add_f32_e64 v62, v62, v64
	v_add_f32_e64 v63, v63, v65
	v_sub_u32_e32 v7, v6, v7
	v_fma_f32 v62, v62, s0, v180
	v_fma_f32 v63, v63, s0, v180
	v_subrev_u32_e32 v2, s7, v2
	v_mul_f32_e32 v64, 0x4b800000, v63
	v_cmp_gt_f32_e64 s[48:49], s33, v63
	v_cmp_gt_f32_e64 s[46:47], s33, v62
	s_movk_i32 s0, 0xff
	v_cndmask_b32_e64 v63, v63, v64, s[48:49]
	v_rsq_f32_e32 v63, v63
	v_lshlrev_b32_e32 v2, 10, v2
	v_subrev_u32_e32 v57, s7, v57
	v_lshlrev_b32_e32 v57, 10, v57
	v_mul_f32_e32 v64, 0x45800000, v63
	v_cndmask_b32_e64 v102, v63, v64, s[48:49]
	v_mul_f32_e32 v63, 0x4b800000, v62
	v_cndmask_b32_e64 v62, v62, v63, s[46:47]
	v_rsq_f32_e32 v62, v62
	v_mul_f32_e64 v70, v102, v72
	v_mul_f32_e64 v71, v102, v73
	v_mul_f32_e64 v72, v102, v76
	v_mul_f32_e64 v73, v102, v77
	v_cmp_le_i32_e32 vcc, s20, v74
	v_mul_f32_e32 v63, 0x45800000, v62
	v_cndmask_b32_e64 v100, v62, v63, s[46:47]
	v_cmp_lt_i32_e64 s[46:47], s0, v7
	v_mul_f32_e64 v60, v100, v60
	v_mul_f32_e64 v61, v100, v61
	v_mul_f32_e64 v58, v100, v58
	v_mul_f32_e64 v59, v100, v59
	v_cndmask_b32_e64 v2, v212, v2, s[46:47]
	v_lshlrev_b32_e32 v2, 2, v2
	v_add_u32_e32 v7, v33, v2
	ds_read_b128 v[62:65], v7
	v_add_u32_e32 v7, v31, v2
	ds_read_b128 v[66:69], v7
	v_cmp_lt_i32_e64 s[46:47], s0, v75
	v_ashrrev_i32_e32 v7, 31, v6
	v_lshlrev_b64 v[120:121], 11, v[6:7]
	v_cndmask_b32_e64 v57, v212, v57, s[46:47]
	s_waitcnt lgkmcnt(0)
	v_fma_f32 v122, v68, v72, v64
	v_fma_f32 v123, v69, v73, v65
	v_fma_f32 v126, v66, v70, v62
	v_fma_f32 v127, v67, v71, v63
	v_lshlrev_b32_e32 v143, 2, v57
	v_lshl_add_u64 v[62:63], v[26:27], 0, v[120:121]
	v_cvt_pk_bf16_f32 v64, v126, v127
	v_cvt_pk_bf16_f32 v65, v122, v123
	v_add_u32_e32 v57, v31, v143
	global_store_dwordx2 v[62:63], v[64:65], off
	ds_read_b128 v[62:65], v57
	v_add_u32_e32 v57, v33, v143
	ds_read_b128 v[66:69], v57
	s_waitcnt lgkmcnt(0)
	v_fma_f32 v124, v64, v58, v68
	v_fma_f32 v125, v65, v59, v69
	v_fma_f32 v128, v62, v60, v66
	v_fma_f32 v129, v63, v61, v67
	s_and_saveexec_b64 s[0:1], vcc
	s_xor_b64 s[0:1], exec, s[0:1]
	s_or_saveexec_b64 s[0:1], s[0:1]
	v_ashrrev_i32_e32 v75, 31, v74
	s_xor_b64 exec, exec, s[0:1]
	s_cbranch_execz .LBB0_1538
	v_lshlrev_b64 v[58:59], 11, v[74:75]
	v_lshl_add_u64 v[58:59], v[26:27], 0, v[58:59]
	v_cvt_pk_bf16_f32 v60, v128, v129
	v_cvt_pk_bf16_f32 v61, v124, v125
	global_store_dwordx2 v[58:59], v[60:61], off
.LBB0_1538:
	s_or_b64 exec, exec, s[0:1]
	ds_read_b128 v[62:65], v130
	ds_read_b128 v[68:71], v130 offset:16
	ds_read_b128 v[144:147], v130 offset:32
	ds_read_b128 v[148:151], v130 offset:48
	s_mov_b32 s30, s31
	v_mov_b64_e32 v[82:83], s[30:31]
	v_mov_b64_e32 v[66:67], s[30:31]
	s_waitcnt lgkmcnt(3)
	v_fma_f32 v82, v126, v62, v82
	v_fma_f32 v83, v126, v63, v83
	v_mov_b64_e32 v[78:79], s[30:31]
	v_fma_f32 v66, v128, v62, v66
	v_fma_f32 v67, v128, v63, v67
	v_mov_b64_e32 v[62:63], s[30:31]
	v_fma_f32 v78, v126, v64, v78
	v_fma_f32 v79, v126, v65, v79
	v_fma_f32 v62, v128, v64, v62
	v_fma_f32 v63, v128, v65, v63
	v_mov_b64_e32 v[80:81], s[30:31]
	v_mov_b64_e32 v[64:65], s[30:31]
	s_waitcnt lgkmcnt(2)
	v_fma_f32 v80, v126, v68, v80
	v_fma_f32 v81, v126, v69, v81
	v_fma_f32 v64, v128, v68, v64
	v_fma_f32 v65, v128, v69, v65
	v_mov_b64_e32 v[90:91], s[30:31]
	v_mov_b64_e32 v[86:87], s[30:31]
	v_mov_b64_e32 v[72:73], s[30:31]
	v_mov_b64_e32 v[68:69], s[30:31]
	v_mov_b64_e32 v[76:77], s[30:31]
	v_mov_b64_e32 v[60:61], s[30:31]
	s_waitcnt lgkmcnt(1)
	v_fma_f32 v90, v126, v144, v90
	v_fma_f32 v91, v126, v145, v91
	v_fma_f32 v86, v126, v146, v86
	v_fma_f32 v87, v126, v147, v87
	v_fma_f32 v72, v128, v144, v72
	v_fma_f32 v73, v128, v145, v73
	v_fma_f32 v68, v128, v146, v68
	v_fma_f32 v69, v128, v147, v69
	ds_read_b128 v[144:147], v130 offset:20480
	v_mov_b64_e32 v[58:59], s[30:31]
	v_fma_f32 v76, v126, v70, v76
	v_fma_f32 v77, v126, v71, v77
	v_fma_f32 v60, v128, v70, v60
	v_fma_f32 v61, v128, v71, v61
	v_mov_b64_e32 v[88:89], s[30:31]
	v_mov_b64_e32 v[84:85], s[30:31]
	v_mov_b64_e32 v[70:71], s[30:31]
	s_waitcnt lgkmcnt(0)
	v_fma_f32 v82, v127, v144, v82
	v_fma_f32 v83, v127, v145, v83
	v_fma_f32 v78, v127, v146, v78
	v_fma_f32 v79, v127, v147, v79
	v_fma_f32 v66, v129, v144, v66
	v_fma_f32 v67, v129, v145, v67
	v_fma_f32 v62, v129, v146, v62
	v_fma_f32 v63, v129, v147, v63
	ds_read_b128 v[144:147], v130 offset:20496
	v_fma_f32 v88, v126, v148, v88
	v_fma_f32 v89, v126, v149, v89
	v_fma_f32 v84, v126, v150, v84
	v_fma_f32 v85, v126, v151, v85
	v_fma_f32 v70, v128, v148, v70
	v_fma_f32 v71, v128, v149, v71
	v_fma_f32 v58, v128, v150, v58
	v_fma_f32 v59, v128, v151, v59
	s_waitcnt lgkmcnt(0)
	v_fma_f32 v80, v127, v144, v80
	v_fma_f32 v81, v127, v145, v81
	v_fma_f32 v76, v127, v146, v76
	v_fma_f32 v77, v127, v147, v77
	v_fma_f32 v64, v129, v144, v64
	v_fma_f32 v65, v129, v145, v65
	v_fma_f32 v60, v129, v146, v60
	v_fma_f32 v61, v129, v147, v61
	ds_read_b128 v[144:147], v130 offset:20512
	s_waitcnt lgkmcnt(0)
	v_fma_f32 v90, v127, v144, v90
	v_fma_f32 v91, v127, v145, v91
	v_fma_f32 v86, v127, v146, v86
	v_fma_f32 v87, v127, v147, v87
	v_fma_f32 v72, v129, v144, v72
	v_fma_f32 v73, v129, v145, v73
	v_fma_f32 v68, v129, v146, v68
	v_fma_f32 v69, v129, v147, v69
	ds_read_b128 v[144:147], v130 offset:20528
	s_waitcnt lgkmcnt(0)
	v_fma_f32 v88, v127, v144, v88
	v_fma_f32 v89, v127, v145, v89
	v_fma_f32 v84, v127, v146, v84
	v_fma_f32 v85, v127, v147, v85
	v_fma_f32 v70, v129, v144, v70
	v_fma_f32 v71, v129, v145, v71
	v_fma_f32 v58, v129, v146, v58
	v_fma_f32 v59, v129, v147, v59
	ds_read_b128 v[126:129], v130 offset:40960
	s_waitcnt lgkmcnt(0)
	v_fma_f32 v82, v122, v126, v82
	v_fma_f32 v83, v122, v127, v83
	v_fma_f32 v78, v122, v128, v78
	v_fma_f32 v79, v122, v129, v79
	v_fma_f32 v66, v124, v126, v66
	v_fma_f32 v67, v124, v127, v67
	v_fma_f32 v62, v124, v128, v62
	v_fma_f32 v63, v124, v129, v63
	ds_read_b128 v[126:129], v130 offset:40976
	s_waitcnt lgkmcnt(0)
	v_fma_f32 v80, v122, v126, v80
	v_fma_f32 v81, v122, v127, v81
	v_fma_f32 v76, v122, v128, v76
	v_fma_f32 v77, v122, v129, v77
	v_fma_f32 v64, v124, v126, v64
	v_fma_f32 v65, v124, v127, v65
	v_fma_f32 v60, v124, v128, v60
	v_fma_f32 v61, v124, v129, v61
	ds_read_b128 v[126:129], v130 offset:40992
	s_waitcnt lgkmcnt(0)
	v_fma_f32 v90, v122, v126, v90
	v_fma_f32 v91, v122, v127, v91
	v_fma_f32 v86, v122, v128, v86
	v_fma_f32 v87, v122, v129, v87
	v_fma_f32 v72, v124, v126, v72
	v_fma_f32 v73, v124, v127, v73
	v_fma_f32 v68, v124, v128, v68
	v_fma_f32 v69, v124, v129, v69
	ds_read_b128 v[126:129], v130 offset:41008
	s_waitcnt lgkmcnt(0)
	v_fma_f32 v88, v122, v126, v88
	v_fma_f32 v89, v122, v127, v89
	v_fma_f32 v84, v122, v128, v84
	v_fma_f32 v85, v122, v129, v85
	v_fma_f32 v70, v124, v126, v70
	v_fma_f32 v71, v124, v127, v71
	v_fma_f32 v58, v124, v128, v58
	v_fma_f32 v59, v124, v129, v59
	ds_read_b128 v[126:129], v130 offset:61440
	s_waitcnt lgkmcnt(0)
	v_fma_f32 v82, v123, v126, v82
	v_fma_f32 v83, v123, v127, v83
	v_fma_f32 v78, v123, v128, v78
	v_fma_f32 v79, v123, v129, v79
	v_fma_f32 v66, v125, v126, v66
	v_fma_f32 v67, v125, v127, v67
	v_fma_f32 v62, v125, v128, v62
	v_fma_f32 v63, v125, v129, v63
	ds_read_b128 v[126:129], v130 offset:61456
	s_waitcnt lgkmcnt(0)
	v_fma_f32 v80, v123, v126, v80
	v_fma_f32 v81, v123, v127, v81
	v_fma_f32 v76, v123, v128, v76
	v_fma_f32 v77, v123, v129, v77
	v_fma_f32 v64, v125, v126, v64
	v_fma_f32 v65, v125, v127, v65
	v_fma_f32 v60, v125, v128, v60
	v_fma_f32 v61, v125, v129, v61
	ds_read_b128 v[126:129], v130 offset:61472
	v_readlane_b32 s0, v254, 61
	s_waitcnt lgkmcnt(0)
	v_fma_f32 v90, v123, v126, v90
	v_fma_f32 v91, v123, v127, v91
	v_fma_f32 v86, v123, v128, v86
	v_fma_f32 v87, v123, v129, v87
	v_fma_f32 v72, v125, v126, v72
	v_fma_f32 v73, v125, v127, v73
	v_fma_f32 v68, v125, v128, v68
	v_fma_f32 v69, v125, v129, v69
	ds_read_b128 v[126:129], v130 offset:61488
	s_waitcnt lgkmcnt(0)
	v_fma_f32 v70, v125, v126, v70
	v_fma_f32 v71, v125, v127, v71
	v_fma_f32 v58, v125, v128, v58
	v_fma_f32 v59, v125, v129, v59
	v_add_u32_e32 v57, s0, v2
	v_lshlrev_b32_e32 v125, 2, v28
	v_add_u32_e32 v124, s21, v2
	v_fma_f32 v88, v123, v126, v88
	v_fma_f32 v89, v123, v127, v89
	v_fma_f32 v84, v123, v128, v84
	v_fma_f32 v85, v123, v129, v85
	v_add_u32_e32 v122, v57, v125
	v_add_u32_e32 v2, v124, v125
	ds_read_b128 v[126:129], v122
	ds_read_b128 v[144:147], v2
	v_mov_b32_e32 v103, v102
	v_mov_b32_e32 v122, v102
	v_mov_b32_e32 v123, v102
	v_mul_f32_e64 v118, v122, v118
	v_mul_f32_e64 v119, v123, v119
	v_mul_f32_e64 v116, v102, v116
	v_mul_f32_e64 v117, v103, v117
	s_waitcnt lgkmcnt(0)
	v_fma_f32 v118, v118, v146, v128
	v_fma_f32 v119, v119, v147, v129
	v_fma_f32 v122, v116, v144, v126
	v_fma_f32 v123, v117, v145, v127
	v_lshl_add_u64 v[116:117], s[14:15], 0, v[120:121]
	v_lshlrev_b32_e32 v2, 1, v28
	v_lshl_add_u64 v[120:121], v[116:117], 0, v[2:3]
	v_cvt_pk_bf16_f32 v126, v122, v123
	v_cvt_pk_bf16_f32 v127, v118, v119
	global_store_dwordx2 v[120:121], v[126:127], off
	v_add_u32_e32 v120, s21, v143
	v_add_u32_e32 v2, v120, v125
	v_add_u32_e32 v121, s0, v143
	ds_read_b128 v[126:129], v2
	v_add_u32_e32 v2, v121, v125
	ds_read_b128 v[144:147], v2
	v_mov_b32_e32 v101, v100
	v_mov_b32_e32 v148, v100
	v_mov_b32_e32 v149, v100
	v_mul_f32_e64 v114, v148, v114
	v_mul_f32_e64 v115, v149, v115
	v_mul_f32_e64 v148, v100, v112
	v_mul_f32_e64 v149, v101, v113
	s_waitcnt lgkmcnt(0)
	v_fma_f32 v112, v114, v128, v146
	v_fma_f32 v113, v115, v129, v147
	v_fma_f32 v114, v148, v126, v144
	v_fma_f32 v115, v149, v127, v145
	s_and_saveexec_b64 s[0:1], vcc
	s_xor_b64 s[0:1], exec, s[0:1]
	s_andn2_saveexec_b64 s[0:1], s[0:1]
	s_cbranch_execz .LBB0_1540
	v_lshlrev_b64 v[126:127], 11, v[74:75]
	v_lshl_add_u64 v[126:127], v[34:35], 0, v[126:127]
	v_cvt_pk_bf16_f32 v128, v114, v115
	v_cvt_pk_bf16_f32 v129, v112, v113
	global_store_dwordx2 v[126:127], v[128:129], off
.LBB0_1540:
	s_or_b64 exec, exec, s[0:1]
	ds_read_b128 v[126:129], v130 offset:5120
	ds_read_b128 v[144:147], v130 offset:5136
	ds_read_b128 v[148:151], v130 offset:5152
	ds_read_b128 v[152:155], v130 offset:5168
	s_waitcnt lgkmcnt(3)
	v_fma_f32 v82, v122, v126, v82
	v_fma_f32 v83, v122, v127, v83
	v_fma_f32 v78, v122, v128, v78
	v_fma_f32 v79, v122, v129, v79
	v_fma_f32 v66, v114, v126, v66
	v_fma_f32 v67, v114, v127, v67
	v_fma_f32 v62, v114, v128, v62
	v_fma_f32 v63, v114, v129, v63
	s_waitcnt lgkmcnt(2)
	v_fma_f32 v80, v122, v144, v80
	v_fma_f32 v81, v122, v145, v81
	v_fma_f32 v76, v122, v146, v76
	v_fma_f32 v77, v122, v147, v77
	v_fma_f32 v64, v114, v144, v64
	v_fma_f32 v65, v114, v145, v65
	v_fma_f32 v60, v114, v146, v60
	v_fma_f32 v61, v114, v147, v61
	ds_read_b128 v[126:129], v130 offset:25600
	ds_read_b128 v[144:147], v130 offset:25616
	s_waitcnt lgkmcnt(3)
	v_fma_f32 v90, v122, v148, v90
	v_fma_f32 v91, v122, v149, v91
	v_fma_f32 v86, v122, v150, v86
	v_fma_f32 v87, v122, v151, v87
	v_fma_f32 v72, v114, v148, v72
	v_fma_f32 v73, v114, v149, v73
	v_fma_f32 v68, v114, v150, v68
	v_fma_f32 v69, v114, v151, v69
	s_waitcnt lgkmcnt(2)
	v_fma_f32 v88, v122, v152, v88
	v_fma_f32 v89, v122, v153, v89
	v_fma_f32 v84, v122, v154, v84
	v_fma_f32 v85, v122, v155, v85
	v_fma_f32 v70, v114, v152, v70
	v_fma_f32 v71, v114, v153, v71
	v_fma_f32 v58, v114, v154, v58
	v_fma_f32 v59, v114, v155, v59
	s_waitcnt lgkmcnt(1)
	v_fma_f32 v82, v123, v126, v82
	v_fma_f32 v83, v123, v127, v83
	v_fma_f32 v78, v123, v128, v78
	v_fma_f32 v79, v123, v129, v79
	v_fma_f32 v66, v115, v126, v66
	v_fma_f32 v67, v115, v127, v67
	v_fma_f32 v62, v115, v128, v62
	v_fma_f32 v63, v115, v129, v63
	s_waitcnt lgkmcnt(0)
	v_fma_f32 v80, v123, v144, v80
	v_fma_f32 v81, v123, v145, v81
	ds_read_b128 v[126:129], v130 offset:25632
	v_fma_f32 v76, v123, v146, v76
	v_fma_f32 v77, v123, v147, v77
	v_fma_f32 v64, v115, v144, v64
	v_fma_f32 v65, v115, v145, v65
	v_fma_f32 v60, v115, v146, v60
	v_fma_f32 v61, v115, v147, v61
	ds_read_b128 v[144:147], v130 offset:25648
	s_waitcnt lgkmcnt(1)
	v_fma_f32 v90, v123, v126, v90
	v_fma_f32 v91, v123, v127, v91
	v_fma_f32 v86, v123, v128, v86
	v_fma_f32 v87, v123, v129, v87
	v_fma_f32 v72, v115, v126, v72
	v_fma_f32 v73, v115, v127, v73
	v_fma_f32 v68, v115, v128, v68
	v_fma_f32 v69, v115, v129, v69
	s_waitcnt lgkmcnt(0)
	v_fma_f32 v88, v123, v144, v88
	v_fma_f32 v89, v123, v145, v89
	ds_read_b128 v[126:129], v130 offset:46080
	v_fma_f32 v84, v123, v146, v84
	v_fma_f32 v85, v123, v147, v85
	v_fma_f32 v70, v115, v144, v70
	v_fma_f32 v71, v115, v145, v71
	v_fma_f32 v58, v115, v146, v58
	v_fma_f32 v59, v115, v147, v59
	ds_read_b128 v[144:147], v130 offset:46096
	s_waitcnt lgkmcnt(1)
	v_fma_f32 v82, v118, v126, v82
	v_fma_f32 v83, v118, v127, v83
	v_fma_f32 v78, v118, v128, v78
	v_fma_f32 v79, v118, v129, v79
	v_fma_f32 v66, v112, v126, v66
	v_fma_f32 v67, v112, v127, v67
	v_fma_f32 v62, v112, v128, v62
	v_fma_f32 v63, v112, v129, v63
	s_waitcnt lgkmcnt(0)
	v_fma_f32 v80, v118, v144, v80
	v_fma_f32 v81, v118, v145, v81
	ds_read_b128 v[126:129], v130 offset:46112
	v_fma_f32 v76, v118, v146, v76
	v_fma_f32 v77, v118, v147, v77
	v_fma_f32 v64, v112, v144, v64
	v_fma_f32 v65, v112, v145, v65
	v_fma_f32 v60, v112, v146, v60
	v_fma_f32 v61, v112, v147, v61
	ds_read_b128 v[144:147], v130 offset:46128
	s_waitcnt lgkmcnt(1)
	v_fma_f32 v90, v118, v126, v90
	v_fma_f32 v91, v118, v127, v91
	v_fma_f32 v86, v118, v128, v86
	v_fma_f32 v87, v118, v129, v87
	v_fma_f32 v72, v112, v126, v72
	v_fma_f32 v73, v112, v127, v73
	v_fma_f32 v68, v112, v128, v68
	v_fma_f32 v69, v112, v129, v69
	s_waitcnt lgkmcnt(0)
	v_fma_f32 v88, v118, v144, v88
	v_fma_f32 v89, v118, v145, v89
	ds_read_b128 v[126:129], v131
	v_fma_f32 v84, v118, v146, v84
	v_fma_f32 v85, v118, v147, v85
	v_fma_f32 v70, v112, v144, v70
	v_fma_f32 v71, v112, v145, v71
	v_fma_f32 v58, v112, v146, v58
	v_fma_f32 v59, v112, v147, v59
	ds_read_b128 v[144:147], v132
	v_lshlrev_b32_e32 v122, 2, v30
	s_waitcnt lgkmcnt(1)
	v_fma_f32 v82, v119, v126, v82
	v_fma_f32 v83, v119, v127, v83
	v_fma_f32 v78, v119, v128, v78
	v_fma_f32 v79, v119, v129, v79
	v_fma_f32 v66, v113, v126, v66
	v_fma_f32 v67, v113, v127, v67
	v_fma_f32 v62, v113, v128, v62
	v_fma_f32 v63, v113, v129, v63
	s_waitcnt lgkmcnt(0)
	v_fma_f32 v80, v119, v144, v80
	v_fma_f32 v81, v119, v145, v81
	ds_read_b128 v[126:129], v133
	v_fma_f32 v76, v119, v146, v76
	v_fma_f32 v77, v119, v147, v77
	v_fma_f32 v64, v113, v144, v64
	v_fma_f32 v65, v113, v145, v65
	v_fma_f32 v60, v113, v146, v60
	v_fma_f32 v61, v113, v147, v61
	ds_read_b128 v[144:147], v134
	v_add_u32_e32 v2, v57, v122
	s_waitcnt lgkmcnt(1)
	v_fma_f32 v90, v119, v126, v90
	v_fma_f32 v91, v119, v127, v91
	v_fma_f32 v86, v119, v128, v86
	v_fma_f32 v87, v119, v129, v87
	v_fma_f32 v72, v113, v126, v72
	v_fma_f32 v73, v113, v127, v73
	v_fma_f32 v68, v113, v128, v68
	v_fma_f32 v69, v113, v129, v69
	s_waitcnt lgkmcnt(0)
	v_fma_f32 v88, v119, v144, v88
	v_fma_f32 v89, v119, v145, v89
	v_fma_f32 v84, v119, v146, v84
	v_fma_f32 v85, v119, v147, v85
	v_fma_f32 v70, v113, v144, v70
	v_fma_f32 v71, v113, v145, v71
	v_fma_f32 v58, v113, v146, v58
	v_fma_f32 v59, v113, v147, v59
	v_add_u32_e32 v118, v124, v122
	ds_read_b128 v[112:115], v2
	ds_read_b128 v[126:129], v118
	v_mov_b32_e32 v118, v102
	v_mov_b32_e32 v119, v102
	v_mul_f32_e64 v110, v118, v110
	v_mul_f32_e64 v111, v119, v111
	v_mul_f32_e64 v118, v102, v108
	v_mul_f32_e64 v119, v103, v109
	s_waitcnt lgkmcnt(0)
	v_fma_f32 v108, v110, v128, v114
	v_fma_f32 v109, v111, v129, v115
	v_fma_f32 v110, v118, v126, v112
	v_fma_f32 v111, v119, v127, v113
	v_lshlrev_b32_e32 v2, 1, v30
	v_lshl_add_u64 v[112:113], v[116:117], 0, v[2:3]
	v_cvt_pk_bf16_f32 v114, v110, v111
	v_cvt_pk_bf16_f32 v115, v108, v109
	global_store_dwordx2 v[112:113], v[114:115], off
	v_add_u32_e32 v2, v120, v122
	v_add_u32_e32 v118, v121, v122
	ds_read_b128 v[112:115], v2
	ds_read_b128 v[126:129], v118
	v_mov_b32_e32 v118, v100
	v_mov_b32_e32 v119, v100
	v_mul_f32_e64 v106, v118, v106
	v_mul_f32_e64 v107, v119, v107
	v_mul_f32_e64 v118, v100, v104
	v_mul_f32_e64 v119, v101, v105
	s_waitcnt lgkmcnt(0)
	v_fma_f32 v104, v106, v114, v128
	v_fma_f32 v105, v107, v115, v129
	v_fma_f32 v106, v118, v112, v126
	v_fma_f32 v107, v119, v113, v127
	s_and_saveexec_b64 s[0:1], vcc
	s_xor_b64 s[0:1], exec, s[0:1]
	s_andn2_saveexec_b64 s[0:1], s[0:1]
	s_cbranch_execz .LBB0_1542
	v_lshlrev_b64 v[112:113], 11, v[74:75]
	v_lshl_add_u64 v[112:113], v[36:37], 0, v[112:113]
	v_cvt_pk_bf16_f32 v114, v106, v107
	v_cvt_pk_bf16_f32 v115, v104, v105
	global_store_dwordx2 v[112:113], v[114:115], off
.LBB0_1542:
	s_or_b64 exec, exec, s[0:1]
	ds_read_b128 v[112:115], v130 offset:10240
	ds_read_b128 v[126:129], v130 offset:10256
	ds_read_b128 v[144:147], v130 offset:10272
	ds_read_b128 v[148:151], v130 offset:10288
	s_waitcnt lgkmcnt(3)
	v_fma_f32 v82, v110, v112, v82
	v_fma_f32 v83, v110, v113, v83
	v_fma_f32 v78, v110, v114, v78
	v_fma_f32 v79, v110, v115, v79
	v_fma_f32 v66, v106, v112, v66
	v_fma_f32 v67, v106, v113, v67
	v_fma_f32 v62, v106, v114, v62
	v_fma_f32 v63, v106, v115, v63
	s_waitcnt lgkmcnt(2)
	v_fma_f32 v80, v110, v126, v80
	v_fma_f32 v81, v110, v127, v81
	v_fma_f32 v76, v110, v128, v76
	v_fma_f32 v77, v110, v129, v77
	v_fma_f32 v64, v106, v126, v64
	v_fma_f32 v65, v106, v127, v65
	v_fma_f32 v60, v106, v128, v60
	v_fma_f32 v61, v106, v129, v61
	ds_read_b128 v[112:115], v130 offset:30720
	ds_read_b128 v[126:129], v130 offset:30736
	s_waitcnt lgkmcnt(3)
	v_fma_f32 v90, v110, v144, v90
	v_fma_f32 v91, v110, v145, v91
	v_fma_f32 v86, v110, v146, v86
	v_fma_f32 v87, v110, v147, v87
	v_fma_f32 v72, v106, v144, v72
	v_fma_f32 v73, v106, v145, v73
	v_fma_f32 v68, v106, v146, v68
	v_fma_f32 v69, v106, v147, v69
	s_waitcnt lgkmcnt(2)
	v_fma_f32 v88, v110, v148, v88
	v_fma_f32 v89, v110, v149, v89
	v_fma_f32 v84, v110, v150, v84
	v_fma_f32 v85, v110, v151, v85
	v_fma_f32 v70, v106, v148, v70
	v_fma_f32 v71, v106, v149, v71
	v_fma_f32 v58, v106, v150, v58
	v_fma_f32 v59, v106, v151, v59
	s_waitcnt lgkmcnt(1)
	v_fma_f32 v82, v111, v112, v82
	v_fma_f32 v83, v111, v113, v83
	v_fma_f32 v78, v111, v114, v78
	v_fma_f32 v79, v111, v115, v79
	v_fma_f32 v66, v107, v112, v66
	v_fma_f32 v67, v107, v113, v67
	v_fma_f32 v62, v107, v114, v62
	v_fma_f32 v63, v107, v115, v63
	s_waitcnt lgkmcnt(0)
	v_fma_f32 v80, v111, v126, v80
	v_fma_f32 v81, v111, v127, v81
	ds_read_b128 v[112:115], v130 offset:30752
	v_fma_f32 v76, v111, v128, v76
	v_fma_f32 v77, v111, v129, v77
	v_fma_f32 v64, v107, v126, v64
	v_fma_f32 v65, v107, v127, v65
	v_fma_f32 v60, v107, v128, v60
	v_fma_f32 v61, v107, v129, v61
	ds_read_b128 v[126:129], v130 offset:30768
	s_waitcnt lgkmcnt(1)
	v_fma_f32 v90, v111, v112, v90
	v_fma_f32 v91, v111, v113, v91
	v_fma_f32 v86, v111, v114, v86
	v_fma_f32 v87, v111, v115, v87
	v_fma_f32 v72, v107, v112, v72
	v_fma_f32 v73, v107, v113, v73
	v_fma_f32 v68, v107, v114, v68
	v_fma_f32 v69, v107, v115, v69
	s_waitcnt lgkmcnt(0)
	v_fma_f32 v88, v111, v126, v88
	v_fma_f32 v89, v111, v127, v89
	ds_read_b128 v[112:115], v130 offset:51200
	v_fma_f32 v84, v111, v128, v84
	v_fma_f32 v85, v111, v129, v85
	v_fma_f32 v70, v107, v126, v70
	v_fma_f32 v71, v107, v127, v71
	v_fma_f32 v58, v107, v128, v58
	v_fma_f32 v59, v107, v129, v59
	ds_read_b128 v[126:129], v130 offset:51216
	s_waitcnt lgkmcnt(1)
	v_fma_f32 v82, v108, v112, v82
	v_fma_f32 v83, v108, v113, v83
	v_fma_f32 v66, v104, v112, v66
	v_fma_f32 v67, v104, v113, v67
	s_waitcnt lgkmcnt(0)
	v_fma_f32 v80, v108, v126, v80
	v_fma_f32 v81, v108, v127, v81
	ds_read_b128 v[110:113], v130 offset:51232
	v_fma_f32 v76, v108, v128, v76
	v_fma_f32 v77, v108, v129, v77
	v_fma_f32 v64, v104, v126, v64
	v_fma_f32 v65, v104, v127, v65
	v_fma_f32 v60, v104, v128, v60
	v_fma_f32 v61, v104, v129, v61
	ds_read_b128 v[126:129], v130 offset:51248
	v_fma_f32 v78, v108, v114, v78
	v_fma_f32 v79, v108, v115, v79
	v_fma_f32 v62, v104, v114, v62
	v_fma_f32 v63, v104, v115, v63
	s_waitcnt lgkmcnt(1)
	v_fma_f32 v90, v108, v110, v90
	v_fma_f32 v91, v108, v111, v91
	v_fma_f32 v86, v108, v112, v86
	v_fma_f32 v87, v108, v113, v87
	v_fma_f32 v72, v104, v110, v72
	v_fma_f32 v73, v104, v111, v73
	v_fma_f32 v68, v104, v112, v68
	v_fma_f32 v69, v104, v113, v69
	s_waitcnt lgkmcnt(0)
	v_fma_f32 v88, v108, v126, v88
	v_fma_f32 v89, v108, v127, v89
	ds_read_b128 v[110:113], v135
	v_fma_f32 v84, v108, v128, v84
	v_fma_f32 v85, v108, v129, v85
	v_fma_f32 v70, v104, v126, v70
	v_fma_f32 v71, v104, v127, v71
	v_fma_f32 v58, v104, v128, v58
	v_fma_f32 v59, v104, v129, v59
	ds_read_b128 v[126:129], v136
	v_lshlrev_b32_e32 v114, 2, v32
	s_waitcnt lgkmcnt(1)
	v_fma_f32 v82, v109, v110, v82
	v_fma_f32 v83, v109, v111, v83
	v_fma_f32 v78, v109, v112, v78
	v_fma_f32 v79, v109, v113, v79
	v_fma_f32 v66, v105, v110, v66
	v_fma_f32 v67, v105, v111, v67
	v_fma_f32 v62, v105, v112, v62
	v_fma_f32 v63, v105, v113, v63
	s_waitcnt lgkmcnt(0)
	v_fma_f32 v80, v109, v126, v80
	v_fma_f32 v81, v109, v127, v81
	ds_read_b128 v[110:113], v137
	v_fma_f32 v76, v109, v128, v76
	v_fma_f32 v77, v109, v129, v77
	v_fma_f32 v64, v105, v126, v64
	v_fma_f32 v65, v105, v127, v65
	v_fma_f32 v60, v105, v128, v60
	v_fma_f32 v61, v105, v129, v61
	ds_read_b128 v[126:129], v138
	v_add_u32_e32 v2, v57, v114
	s_waitcnt lgkmcnt(1)
	v_fma_f32 v90, v109, v110, v90
	v_fma_f32 v91, v109, v111, v91
	v_fma_f32 v86, v109, v112, v86
	v_fma_f32 v87, v109, v113, v87
	v_fma_f32 v72, v105, v110, v72
	v_fma_f32 v73, v105, v111, v73
	v_fma_f32 v68, v105, v112, v68
	v_fma_f32 v69, v105, v113, v69
	s_waitcnt lgkmcnt(0)
	v_fma_f32 v88, v109, v126, v88
	v_fma_f32 v89, v109, v127, v89
	v_fma_f32 v84, v109, v128, v84
	v_fma_f32 v85, v109, v129, v85
	v_fma_f32 v70, v105, v126, v70
	v_fma_f32 v71, v105, v127, v71
	v_fma_f32 v58, v105, v128, v58
	v_fma_f32 v59, v105, v129, v59
	v_add_u32_e32 v57, v124, v114
	ds_read_b128 v[104:107], v2
	ds_read_b128 v[108:111], v57
	v_mov_b32_e32 v112, v102
	v_mov_b32_e32 v113, v102
	v_mul_f32_e64 v98, v112, v98
	v_mul_f32_e64 v99, v113, v99
	v_mul_f32_e64 v102, v102, v96
	v_mul_f32_e64 v103, v103, v97
	s_waitcnt lgkmcnt(0)
	v_fma_f32 v96, v98, v110, v106
	v_fma_f32 v97, v99, v111, v107
	v_fma_f32 v98, v102, v108, v104
	v_fma_f32 v99, v103, v109, v105
	v_lshlrev_b32_e32 v2, 1, v32
	v_lshl_add_u64 v[102:103], v[116:117], 0, v[2:3]
	v_cvt_pk_bf16_f32 v104, v98, v99
	v_cvt_pk_bf16_f32 v105, v96, v97
	global_store_dwordx2 v[102:103], v[104:105], off
	v_add_u32_e32 v2, v120, v114
	v_add_u32_e32 v57, v121, v114
	ds_read_b128 v[102:105], v2
	ds_read_b128 v[106:109], v57
	v_mov_b32_e32 v110, v100
	v_mov_b32_e32 v111, v100
	v_mul_f32_e64 v94, v110, v94
	v_mul_f32_e64 v95, v111, v95
	v_mul_f32_e64 v100, v100, v92
	v_mul_f32_e64 v101, v101, v93
	s_waitcnt lgkmcnt(0)
	v_fma_f32 v92, v94, v104, v108
	v_fma_f32 v93, v95, v105, v109
	v_fma_f32 v94, v100, v102, v106
	v_fma_f32 v95, v101, v103, v107
	s_and_saveexec_b64 s[0:1], vcc
	s_xor_b64 s[0:1], exec, s[0:1]
	s_andn2_saveexec_b64 s[0:1], s[0:1]
	s_cbranch_execz .LBB0_1546
	v_lshlrev_b64 v[74:75], 11, v[74:75]
	v_lshl_add_u64 v[74:75], v[38:39], 0, v[74:75]
	v_cvt_pk_bf16_f32 v100, v94, v95
	v_cvt_pk_bf16_f32 v101, v92, v93
	global_store_dwordx2 v[74:75], v[100:101], off
.LBB0_1546:
	s_or_b64 exec, exec, s[0:1]
	ds_read_b128 v[100:103], v130 offset:15360
	ds_read_b128 v[104:107], v130 offset:15376
	ds_read_b128 v[108:111], v130 offset:15392
	ds_read_b128 v[112:115], v130 offset:15408
	v_and_or_b32 v2, v211, 64, v29
	s_waitcnt lgkmcnt(3)
	v_fma_f32 v82, v98, v100, v82
	v_fma_f32 v83, v98, v101, v83
	v_fma_f32 v78, v98, v102, v78
	v_fma_f32 v79, v98, v103, v79
	v_fma_f32 v66, v94, v100, v66
	v_fma_f32 v67, v94, v101, v67
	v_fma_f32 v62, v94, v102, v62
	v_fma_f32 v63, v94, v103, v63
	ds_read_b128 v[100:103], v130 offset:35840
	s_waitcnt lgkmcnt(3)
	v_fma_f32 v80, v98, v104, v80
	v_fma_f32 v81, v98, v105, v81
	v_fma_f32 v76, v98, v106, v76
	v_fma_f32 v77, v98, v107, v77
	v_fma_f32 v64, v94, v104, v64
	v_fma_f32 v65, v94, v105, v65
	v_fma_f32 v60, v94, v106, v60
	v_fma_f32 v61, v94, v107, v61
	s_waitcnt lgkmcnt(2)
	v_fma_f32 v90, v98, v108, v90
	v_fma_f32 v91, v98, v109, v91
	v_fma_f32 v86, v98, v110, v86
	v_fma_f32 v87, v98, v111, v87
	v_fma_f32 v72, v94, v108, v72
	v_fma_f32 v73, v94, v109, v73
	v_fma_f32 v68, v94, v110, v68
	v_fma_f32 v69, v94, v111, v69
	ds_read_b128 v[104:107], v130 offset:35856
	s_waitcnt lgkmcnt(1)
	v_fma_f32 v82, v99, v100, v82
	v_fma_f32 v83, v99, v101, v83
	v_fma_f32 v78, v99, v102, v78
	v_fma_f32 v79, v99, v103, v79
	v_fma_f32 v66, v95, v100, v66
	v_fma_f32 v67, v95, v101, v67
	v_fma_f32 v62, v95, v102, v62
	v_fma_f32 v63, v95, v103, v63
	ds_read_b128 v[100:103], v130 offset:35872
	v_fma_f32 v88, v98, v112, v88
	v_fma_f32 v89, v98, v113, v89
	v_fma_f32 v84, v98, v114, v84
	v_fma_f32 v85, v98, v115, v85
	v_fma_f32 v70, v94, v112, v70
	v_fma_f32 v71, v94, v113, v71
	v_fma_f32 v58, v94, v114, v58
	v_fma_f32 v59, v94, v115, v59
	s_waitcnt lgkmcnt(1)
	v_fma_f32 v80, v99, v104, v80
	v_fma_f32 v81, v99, v105, v81
	v_fma_f32 v76, v99, v106, v76
	v_fma_f32 v77, v99, v107, v77
	v_fma_f32 v64, v95, v104, v64
	v_fma_f32 v65, v95, v105, v65
	v_fma_f32 v60, v95, v106, v60
	v_fma_f32 v61, v95, v107, v61
	ds_read_b128 v[104:107], v130 offset:35888
	s_waitcnt lgkmcnt(1)
	v_fma_f32 v90, v99, v100, v90
	v_fma_f32 v91, v99, v101, v91
	v_fma_f32 v86, v99, v102, v86
	v_fma_f32 v87, v99, v103, v87
	v_fma_f32 v72, v95, v100, v72
	v_fma_f32 v73, v95, v101, v73
	v_fma_f32 v68, v95, v102, v68
	v_fma_f32 v69, v95, v103, v69
	ds_read_b128 v[100:103], v130 offset:56320
	s_waitcnt lgkmcnt(1)
	v_fma_f32 v88, v99, v104, v88
	v_fma_f32 v89, v99, v105, v89
	v_fma_f32 v84, v99, v106, v84
	v_fma_f32 v85, v99, v107, v85
	v_fma_f32 v70, v95, v104, v70
	v_fma_f32 v71, v95, v105, v71
	v_fma_f32 v58, v95, v106, v58
	v_fma_f32 v59, v95, v107, v59
	ds_read_b128 v[104:107], v130 offset:56336
	s_waitcnt lgkmcnt(1)
	v_fma_f32 v82, v96, v100, v82
	v_fma_f32 v83, v96, v101, v83
	v_fma_f32 v66, v92, v100, v66
	v_fma_f32 v67, v92, v101, v67
	ds_read_b128 v[98:101], v130 offset:56352
	v_fma_f32 v78, v96, v102, v78
	v_fma_f32 v79, v96, v103, v79
	v_fma_f32 v62, v92, v102, v62
	v_fma_f32 v63, v92, v103, v63
	s_waitcnt lgkmcnt(1)
	v_fma_f32 v80, v96, v104, v80
	v_fma_f32 v81, v96, v105, v81
	v_fma_f32 v76, v96, v106, v76
	v_fma_f32 v77, v96, v107, v77
	v_fma_f32 v64, v92, v104, v64
	v_fma_f32 v65, v92, v105, v65
	ds_read_b128 v[102:105], v130 offset:56368
	s_waitcnt lgkmcnt(1)
	v_fma_f32 v90, v96, v98, v90
	v_fma_f32 v91, v96, v99, v91
	v_fma_f32 v86, v96, v100, v86
	v_fma_f32 v87, v96, v101, v87
	v_fma_f32 v72, v92, v98, v72
	v_fma_f32 v73, v92, v99, v73
	v_fma_f32 v68, v92, v100, v68
	v_fma_f32 v69, v92, v101, v69
	s_waitcnt lgkmcnt(0)
	v_fma_f32 v88, v96, v102, v88
	v_fma_f32 v89, v96, v103, v89
	ds_read_b128 v[98:101], v139
	v_fma_f32 v84, v96, v104, v84
	v_fma_f32 v85, v96, v105, v85
	v_fma_f32 v60, v92, v106, v60
	v_fma_f32 v61, v92, v107, v61
	v_fma_f32 v70, v92, v102, v70
	v_fma_f32 v71, v92, v103, v71
	v_fma_f32 v58, v92, v104, v58
	v_fma_f32 v59, v92, v105, v59
	ds_read_b128 v[102:105], v140
	s_waitcnt lgkmcnt(1)
	v_fma_f32 v82, v97, v98, v82
	v_fma_f32 v83, v97, v99, v83
	v_fma_f32 v78, v97, v100, v78
	v_fma_f32 v79, v97, v101, v79
	v_fma_f32 v66, v93, v98, v66
	v_fma_f32 v67, v93, v99, v67
	v_fma_f32 v62, v93, v100, v62
	v_fma_f32 v63, v93, v101, v63
	ds_read_b128 v[98:101], v141
	ds_read_b128 v[106:109], v142
	s_waitcnt lgkmcnt(2)
	v_fma_f32 v80, v97, v102, v80
	v_fma_f32 v81, v97, v103, v81
	v_fma_f32 v76, v97, v104, v76
	v_fma_f32 v77, v97, v105, v77
	s_waitcnt lgkmcnt(1)
	v_fma_f32 v90, v97, v98, v90
	v_fma_f32 v91, v97, v99, v91
	v_fma_f32 v86, v97, v100, v86
	v_fma_f32 v87, v97, v101, v87
	s_waitcnt lgkmcnt(0)
	v_fma_f32 v88, v97, v106, v88
	v_fma_f32 v89, v97, v107, v89
	v_fma_f32 v84, v97, v108, v84
	v_fma_f32 v85, v97, v109, v85
	v_lshlrev_b32_e32 v2, 2, v2
	v_permlane32_swap_b32_e32 v82, v90
	v_permlane32_swap_b32_e32 v83, v91
	v_permlane32_swap_b32_e32 v78, v86
	v_permlane32_swap_b32_e32 v79, v87
	v_permlane32_swap_b32_e32 v80, v88
	v_permlane32_swap_b32_e32 v81, v89
	v_permlane32_swap_b32_e32 v76, v84
	v_permlane32_swap_b32_e32 v77, v85
	v_add_f32_e32 v57, v82, v90
	v_add_f32_e32 v74, v83, v91
	v_add_f32_e32 v75, v78, v86
	v_add_f32_e32 v78, v79, v87
	v_add_f32_e32 v79, v80, v88
	v_add_f32_e32 v80, v81, v89
	v_add_f32_e32 v76, v76, v84
	v_add_f32_e32 v77, v77, v85
	v_permlane16_swap_b32_e32 v57, v79
	v_permlane16_swap_b32_e32 v74, v80
	v_permlane16_swap_b32_e32 v75, v76
	v_permlane16_swap_b32_e32 v78, v77
	v_add_f32_e32 v57, v57, v79
	v_add_f32_e32 v74, v74, v80
	v_add_f32_e32 v75, v75, v76
	v_add_f32_e32 v76, v78, v77
	v_cndmask_b32_e64 v77, v57, v75, s[38:39]
	v_cndmask_b32_e64 v57, v75, v57, s[38:39]
	v_cndmask_b32_e64 v75, v74, v76, s[38:39]
	v_cndmask_b32_e64 v74, v76, v74, s[38:39]
	v_add_f32_dpp v57, v77, v57 row_ror:8 row_mask:0xf bank_mask:0xf bound_ctrl:1
	s_mov_b64 s[0:1], 0
	v_add_f32_dpp v74, v75, v74 row_ror:8 row_mask:0xf bank_mask:0xf bound_ctrl:1
	v_cndmask_b32_e64 v75, v57, v74, s[40:41]
	v_cndmask_b32_e64 v57, v74, v57, s[40:41]
	v_mov_b32_e32 v74, v3
	v_fma_f32 v64, v93, v102, v64
	v_fma_f32 v65, v93, v103, v65
	v_fma_f32 v60, v93, v104, v60
	v_fma_f32 v61, v93, v105, v61
	v_fma_f32 v72, v93, v98, v72
	v_fma_f32 v73, v93, v99, v73
	v_fma_f32 v68, v93, v100, v68
	v_fma_f32 v69, v93, v101, v69
	v_fma_f32 v70, v93, v106, v70
	v_fma_f32 v71, v93, v107, v71
	s_nop 1
	v_mov_b32_dpp v74, v75 row_half_mirror row_mask:0xf bank_mask:0xf
	v_fma_f32 v58, v93, v108, v58
	v_fma_f32 v59, v93, v109, v59
	s_nop 1
	v_add_f32_dpp v57, v74, v57 quad_perm:[3,2,1,0] row_mask:0xf bank_mask:0xf bound_ctrl:1
	v_mov_b32_e32 v74, v3
	s_nop 0
	v_add_f32_dpp v57, v57, v57 quad_perm:[1,0,3,2] row_mask:0xf bank_mask:0xf bound_ctrl:1
	s_nop 1
	v_add_f32_dpp v57, v57, v57 quad_perm:[2,3,0,1] row_mask:0xf bank_mask:0xf bound_ctrl:1
	ds_bpermute_b32 v57, v2, v57
	s_waitcnt lgkmcnt(0)
	v_max_f32_e32 v75, v57, v57
	v_mov_b32_dpp v74, v57 quad_perm:[1,0,3,2] row_mask:0xf bank_mask:0xf
	v_max_f32_e32 v74, v74, v74
	v_max_f32_e32 v74, v75, v74
	v_mov_b32_e32 v75, v3
	s_nop 1
	v_mov_b32_dpp v75, v74 quad_perm:[2,3,0,1] row_mask:0xf bank_mask:0xf
	v_max_f32_e32 v75, v75, v75
	v_max_f32_e32 v74, v74, v75
	v_mov_b32_e32 v75, v3
	s_nop 1
	v_mov_b32_dpp v75, v74 row_ror:4 row_mask:0xf bank_mask:0xf
	v_max_f32_e32 v75, v75, v75
	v_max_f32_e32 v74, v74, v75
	v_mov_b32_e32 v75, v3
	s_nop 1
	v_mov_b32_dpp v75, v74 row_ror:8 row_mask:0xf bank_mask:0xf
	v_max_f32_e32 v75, v75, v75
	v_max_f32_e32 v74, v74, v75
	v_sub_f32_e32 v57, v57, v74
	v_mul_f32_e32 v74, 0x3fb8aa3b, v57
	v_fma_f32 v75, v57, s37, -v74
	v_rndne_f32_e32 v76, v74
	v_fmac_f32_e32 v75, 0x32a5705f, v57
	v_sub_f32_e32 v74, v74, v76
	v_add_f32_e32 v74, v74, v75
	v_exp_f32_e32 v74, v74
	v_cvt_i32_f32_e32 v75, v76
	v_cmp_ngt_f32_e32 vcc, s97, v57
	v_ldexp_f32 v74, v74, v75
	s_nop 0
	v_cndmask_b32_e32 v74, 0, v74, vcc
	v_cmp_nlt_f32_e32 vcc, s10, v57
	v_mov_b32_e32 v75, v3
	s_nop 0
	v_cndmask_b32_e32 v57, v210, v74, vcc
	s_nop 1
	v_add_f32_dpp v74, v57, v57 quad_perm:[1,0,3,2] row_mask:0xf bank_mask:0xf bound_ctrl:1
	s_nop 1
	v_add_f32_dpp v74, v74, v74 quad_perm:[2,3,0,1] row_mask:0xf bank_mask:0xf bound_ctrl:1
	s_nop 1
	v_add_f32_dpp v74, v74, v74 row_ror:4 row_mask:0xf bank_mask:0xf bound_ctrl:1
	s_nop 1
	v_mov_b32_dpp v75, v74 row_ror:8 row_mask:0xf bank_mask:0xf
	s_and_saveexec_b64 s[2:3], s[42:43]
	s_cbranch_execz .LBB0_1548
	v_add_f32_e32 v74, v74, v75
	v_div_scale_f32 v75, s[0:1], v74, v74, v57
	v_rcp_f32_e32 v76, v75
	v_div_scale_f32 v77, vcc, v57, v74, v57
	s_and_b64 s[0:1], s[44:45], exec
	v_fma_f32 v78, -v75, v76, 1.0
	v_fmac_f32_e32 v76, v78, v76
	v_mul_f32_e32 v78, v77, v76
	v_fma_f32 v79, -v75, v78, v77
	v_fmac_f32_e32 v78, v79, v76
	v_fma_f32 v75, -v75, v78, v77
	v_div_fmas_f32 v75, v75, v76, v78
	v_div_fixup_f32 v57, v75, v74, v57
	v_lshlrev_b64 v[74:75], 6, v[6:7]
	v_lshl_or_b32 v74, v4, 2, v74
	v_lshl_add_u64 v[76:77], s[12:13], 0, v[74:75]
	v_lshl_add_u64 v[74:75], s[50:51], 0, v[74:75]
	v_mov_b32_e32 v7, -1
	global_store_dword v[76:77], v57, off
	global_store_dword v[74:75], v7, off
